# C1 + router/weight-copy work queue pops the next slot one item ahead (returning atomic overlaps the current item)
# baseline (speedup 1.0000x reference)
.LBB0_1208:
	s_or_b64 exec, exec, s[8:9]
	v_readlane_b32 s42, v255, 9
	v_readlane_b32 s43, v255, 10
	s_load_dwordx2 s[8:9], s[42:43], 0x38
	v_lshlrev_b32_e32 v2, 2, v1
	v_ashrrev_i32_e32 v3, 31, v2
	s_load_dwordx2 s[30:31], s[42:43], 0x48
	s_load_dwordx2 s[34:35], s[42:43], 0x58
	s_load_dwordx2 s[36:37], s[42:43], 0x70
	v_lshlrev_b32_e32 v13, 4, v1
	s_waitcnt lgkmcnt(0)
	v_lshl_add_u64 v[6:7], v[2:3], 2, s[8:9]
	global_load_dwordx4 v[6:9], v[6:7], off
	v_add_u32_e32 v10, 0, v13
	v_add_u32_e32 v25, 0x1a800, v10
	v_readlane_b32 s24, v255, 2
	s_mul_i32 s2, s24, 0x2200
	s_add_i32 s3, s2, 0
	s_add_u32 s23, s26, 0x3b40000
	s_addc_u32 s29, s27, 0
	v_and_b32_e32 v14, 15, v4
	v_mov_b32_e32 v123, 0
	v_lshlrev_b32_e32 v126, 6, v14
	v_mov_b32_e32 v127, v123
	v_lshl_add_u64 v[130:131], s[12:13], 0, v[126:127]
	v_and_b32_e32 v5, 64, v254
	v_and_b32_e32 v3, 31, v4
	v_ashrrev_i32_e32 v12, 5, v4
	v_ashrrev_i32_e32 v120, 4, v1
	v_xor_b32_e32 v4, 32, v254
	v_add_u32_e32 v20, 64, v5
	v_xor_b32_e32 v15, 1, v254
	v_ashrrev_i32_e32 v121, 31, v120
	v_cmp_lt_i32_e32 vcc, v4, v20
	s_mov_b64 s[14:15], 0x80000
	v_xor_b32_e32 v16, 2, v254
	v_cndmask_b32_e32 v26, v254, v4, vcc
	v_lshl_add_u64 v[4:5], v[120:121], 2, s[26:27]
	v_cmp_lt_i32_e32 vcc, v15, v20
	v_xor_b32_e32 v17, 4, v254
	s_mul_i32 s21, s24, 0x1400
	v_cndmask_b32_e32 v15, v254, v15, vcc
	v_cmp_lt_i32_e32 vcc, v16, v20
	v_lshl_add_u64 v[132:133], v[4:5], 0, s[14:15]
	s_movk_i32 s20, 0x410
	v_xor_b32_e32 v18, 8, v254
	v_cndmask_b32_e32 v16, v254, v16, vcc
	v_cmp_lt_i32_e32 vcc, v17, v20
	s_movk_i32 s22, 0xa0
	v_lshlrev_b32_e32 v122, 12, v3
	v_mul_lo_u32 v21, v120, s20
	v_lshlrev_b32_e32 v23, 4, v12
	v_cndmask_b32_e32 v17, v254, v17, vcc
	v_cmp_lt_i32_e32 vcc, v18, v20
	s_mov_b64 s[16:17], 0x4a80000
	s_mov_b64 s[18:19], 0x4ac0000
	v_and_b32_e32 v19, -16, v1
	v_ashrrev_i32_e32 v119, 31, v118
	v_mad_u32_u24 v22, v3, s20, 0
	v_mul_lo_u32 v24, v1, s22
	v_lshl_add_u64 v[10:11], s[26:27], 0, v[122:123]
	v_add_u32_e32 v21, 0, v21
	v_cndmask_b32_e32 v18, v254, v18, vcc
	s_mov_b32 s51, 0
	v_cmp_eq_u32_e64 s[8:9], 0, v1
	v_lshlrev_b32_e32 v124, 5, v14
	v_cmp_eq_u32_e64 s[10:11], 0, v14
	v_lshl_add_u64 v[128:129], s[48:49], 0, v[126:127]
	v_lshlrev_b32_e32 v121, 2, v26
	v_lshl_add_u64 v[134:135], v[10:11], 0, s[16:17]
	v_lshl_add_u64 v[136:137], v[10:11], 0, s[18:19]
	v_lshlrev_b32_e32 v127, 2, v15
	v_lshlrev_b32_e32 v141, 2, v16
	v_lshlrev_b32_e32 v186, 2, v17
	v_lshlrev_b32_e32 v187, 2, v18
	v_lshl_add_u64 v[138:139], s[40:41], 0, v[118:119]
	v_mul_u32_u24_e32 v119, 0x210, v14
	v_lshlrev_b32_e32 v193, 7, v14
	v_lshl_add_u32 v140, v12, 3, s86
	s_movk_i32 s72, 0x7ff
	s_movk_i32 s73, 0x84
	s_mov_b32 s74, 0x42fe0000
	s_mov_b32 s75, 0xc2fe0000
	s_mov_b32 s76, 0xc0c0500
	s_mov_b32 s77, 0xc3e00000
	s_mov_b32 s78, 0x40c0c00
	s_mov_b32 s79, 0x4b00000
	s_mov_b64 s[60:61], 0x30000400
	s_mov_b64 s[62:63], 0x38000400
	v_add_u32_e32 v194, v21, v126
	s_mov_b64 s[64:65], 0x200
	s_mov_b64 s[66:67], 0x400
	s_waitcnt vmcnt(0)
	ds_write_b128 v25, v[6:9]
	s_waitcnt lgkmcnt(0)
	s_barrier
	s_load_dword s25, s[42:43], 0x98
	v_mov_b32_e32 v197, 0x358637bd
	s_mov_b32 s80, 0xf800000
	v_mov_b32_e32 v198, 0x260
	s_mov_b32 s81, 0xff800000
	s_waitcnt lgkmcnt(0)
	s_cmp_eq_u32 s25, 0
	s_cselect_b32 s2, 0, 0x100
	s_add_u32 s2, s26, s2
	s_addc_u32 s12, s27, 0
	s_add_u32 s54, s2, 0xc3500
	s_addc_u32 s55, s12, 0
	s_lshl_b32 s2, s24, 7
	s_add_i32 s33, s2, 0
	s_add_i32 s33, s33, 0x26000
	v_readlane_b32 s2, v255, 3
	s_cmp_lt_u32 s2, 64
	s_cselect_b64 s[56:57], -1, 0
	s_lshl_b32 s46, s24, 1
	s_add_u32 s58, s26, 0x3b00000
	s_addc_u32 s59, s27, 0
	s_add_i32 s14, 0, 0x10400
	s_lshl_b32 s2, s2, 1
	s_add_i32 s15, s14, s21
	s_add_i32 s13, 0, 0x1a400
	s_and_b32 s2, s2, 0xffffff80
	v_mov_b32_e32 v4, s15
	s_add_i32 s12, 0, 0x1a600
	v_add_u32_e32 v190, s13, v2
	v_add_u32_e32 v2, s2, v23
	v_mad_u32_u24 v3, v3, s22, v4
	s_add_i32 s47, 0, 0x27000
	v_add_u32_e32 v188, s12, v19
	v_lshl_add_u32 v189, v120, 2, s13
	v_add_u32_e32 v191, s12, v13
	v_add_u32_e32 v192, s14, v24
	v_add_u32_e32 v195, v22, v2
	v_add_u32_e32 v196, v3, v23
	v_mov_b32_e32 v199, 1
	s_add_i32 s82, 0, 0x1a500
	v_mov_b32_e32 v200, s47
	v_mov_b32_e32 v201, 0x42fe0000
	v_mov_b32_e32 v202, 0x43e00000
	v_mov_b32_e32 v203, 0xff800000
	s_and_saveexec_b64 s[12:13], s[8:9]
	s_cbranch_execz .Lq10_first
	v_mov_b32_e32 v252, 1
	global_atomic_add v252, v123, v252, s[54:55] sc0
.Lq10_first:
	s_or_b64 exec, exec, s[12:13]
	s_branch .LBB0_1214

.LBB0_1214:
	s_barrier
	s_and_saveexec_b64 s[12:13], s[8:9]
	s_cbranch_execz .LBB0_1218
	s_waitcnt vmcnt(0)
	v_readfirstlane_b32 s2, v252
	v_mov_b32_e32 v3, s47
	s_nop 0
	v_mov_b32_e32 v2, s2
	ds_write_b32 v3, v2
	s_cmp_gt_i32 s2, s72
	s_cbranch_scc1 .Lq10_nopf
	v_mov_b32_e32 v252, 1
	global_atomic_add v252, v123, v252, s[54:55] sc0
.Lq10_nopf:
.LBB0_1218:
	s_or_b64 exec, exec, s[12:13]
	s_waitcnt lgkmcnt(0)
	s_barrier
	ds_read_b32 v2, v200
	s_mov_b64 s[12:13], -1
	s_waitcnt lgkmcnt(0)
	v_cmp_lt_i32_e32 vcc, s72, v2
	v_readfirstlane_b32 s18, v2
	s_cbranch_vccnz .LBB0_1213
	s_bitcmp0_b32 s18, 0
	s_cbranch_scc1 .LBB0_1227
	s_ashr_i32 s16, s18, 1
	s_and_b32 s17, s16, 1
	v_readlane_b32 s14, v255, 9
	v_mov_b32_e32 v4, v254
	s_lshl_b32 s2, s17, 3
	v_readlane_b32 s15, v255, 10
	s_load_dwordx2 s[14:15], s[14:15], s2 offset:0x60
	s_ashr_i32 s12, s18, 6
	s_lshl_b32 s19, s18, 3
	s_ashr_i32 s13, s12, 31
	s_and_b32 s20, s19, 0x1e0
	s_lshl_b64 s[42:43], s[12:13], 22
	s_waitcnt lgkmcnt(0)
	s_add_u32 s2, s14, s42
	v_ashrrev_i32_e32 v20, 5, v4
	s_addc_u32 s15, s15, s43
	v_add_u32_e32 v2, v20, v118
	s_lshl_b32 s14, s20, 2
	v_and_b32_e32 v5, 31, v4
	s_add_u32 s14, s2, s14
	v_add_u32_e32 v16, 8, v2
	s_addc_u32 s15, s15, 0
	v_lshlrev_b32_e32 v122, 2, v5
	v_ashrrev_i32_e32 v17, 31, v16
	v_lshl_add_u64 v[6:7], s[14:15], 0, v[122:123]
	v_lshlrev_b64 v[16:17], 11, v[16:17]
	v_lshl_add_u64 v[22:23], v[6:7], 0, v[16:17]
	v_add_u32_e32 v16, 10, v2
	v_ashrrev_i32_e32 v17, 31, v16
	v_lshlrev_b64 v[16:17], 11, v[16:17]
	v_lshl_add_u64 v[24:25], v[6:7], 0, v[16:17]
	v_add_u32_e32 v16, 12, v2
	v_ashrrev_i32_e32 v17, 31, v16
	v_lshlrev_b64 v[16:17], 11, v[16:17]
	v_add_u32_e32 v12, 4, v2
	v_add_u32_e32 v14, 6, v2
	v_lshl_add_u64 v[26:27], v[6:7], 0, v[16:17]
	v_add_u32_e32 v16, 14, v2
	v_ashrrev_i32_e32 v3, 31, v2
	v_add_u32_e32 v10, 2, v2
	v_ashrrev_i32_e32 v13, 31, v12
	v_ashrrev_i32_e32 v15, 31, v14
	v_ashrrev_i32_e32 v17, 31, v16
	v_lshlrev_b64 v[8:9], 11, v[2:3]
	v_ashrrev_i32_e32 v11, 31, v10
	v_lshlrev_b64 v[12:13], 11, v[12:13]
	v_lshlrev_b64 v[14:15], 11, v[14:15]
	v_lshlrev_b64 v[16:17], 11, v[16:17]
	s_waitcnt vmcnt(1)
	v_add_u32_e32 v30, 28, v2
	v_lshl_add_u64 v[8:9], v[6:7], 0, v[8:9]
	v_lshlrev_b64 v[10:11], 11, v[10:11]
	v_lshl_add_u64 v[12:13], v[6:7], 0, v[12:13]
	v_lshl_add_u64 v[14:15], v[6:7], 0, v[14:15]
	v_lshl_add_u64 v[28:29], v[6:7], 0, v[16:17]
	v_ashrrev_i32_e32 v31, 31, v30
	v_lshl_add_u64 v[10:11], v[6:7], 0, v[10:11]
	global_load_dword v18, v[8:9], off
	global_load_dword v19, v[10:11], off
	global_load_dword v16, v[12:13], off
	global_load_dword v17, v[14:15], off
	s_nop 0
	global_load_dword v14, v[22:23], off
	global_load_dword v15, v[24:25], off
	global_load_dword v12, v[26:27], off
	global_load_dword v13, v[28:29], off
	v_add_u32_e32 v8, 16, v2
	v_add_u32_e32 v24, 22, v2
	v_add_u32_e32 v28, 26, v2
	v_lshlrev_b64 v[30:31], 11, v[30:31]
	v_ashrrev_i32_e32 v9, 31, v8
	v_add_u32_e32 v10, 18, v2
	v_add_u32_e32 v22, 20, v2
	v_ashrrev_i32_e32 v25, 31, v24
	v_add_u32_e32 v26, 24, v2
	v_ashrrev_i32_e32 v29, 31, v28
	v_lshl_add_u64 v[38:39], v[6:7], 0, v[30:31]
	v_add_u32_e32 v30, 30, v2
	v_lshlrev_b64 v[8:9], 11, v[8:9]
	v_ashrrev_i32_e32 v11, 31, v10
	v_ashrrev_i32_e32 v23, 31, v22
	v_lshlrev_b64 v[24:25], 11, v[24:25]
	v_ashrrev_i32_e32 v27, 31, v26
	v_lshlrev_b64 v[28:29], 11, v[28:29]
	v_ashrrev_i32_e32 v31, 31, v30
	v_lshl_add_u64 v[8:9], v[6:7], 0, v[8:9]
	v_lshlrev_b64 v[10:11], 11, v[10:11]
	v_lshlrev_b64 v[22:23], 11, v[22:23]
	v_lshl_add_u64 v[24:25], v[6:7], 0, v[24:25]
	v_lshlrev_b64 v[26:27], 11, v[26:27]
	v_lshl_add_u64 v[28:29], v[6:7], 0, v[28:29]
	v_lshlrev_b64 v[30:31], 11, v[30:31]
	v_lshl_add_u64 v[10:11], v[6:7], 0, v[10:11]
	v_lshl_add_u64 v[22:23], v[6:7], 0, v[22:23]
	v_lshl_add_u64 v[26:27], v[6:7], 0, v[26:27]
	v_lshl_add_u64 v[40:41], v[6:7], 0, v[30:31]
	global_load_dword v35, v[8:9], off
	global_load_dword v36, v[10:11], off
	global_load_dword v33, v[22:23], off
	global_load_dword v34, v[24:25], off
	global_load_dword v31, v[26:27], off
	global_load_dword v32, v[28:29], off
	s_nop 0
	global_load_dword v29, v[38:39], off
	global_load_dword v30, v[40:41], off
	v_add_u32_e32 v8, 32, v2
	v_add_u32_e32 v24, 38, v2
	v_ashrrev_i32_e32 v9, 31, v8
	v_add_u32_e32 v10, 34, v2
	v_add_u32_e32 v22, 36, v2
	v_ashrrev_i32_e32 v25, 31, v24
	v_add_u32_e32 v26, 40, v2
	v_add_u32_e32 v38, 42, v2
	v_add_u32_e32 v40, 44, v2
	v_add_u32_e32 v42, 46, v2
	v_lshlrev_b64 v[8:9], 11, v[8:9]
	v_ashrrev_i32_e32 v11, 31, v10
	v_ashrrev_i32_e32 v23, 31, v22
	v_lshlrev_b64 v[24:25], 11, v[24:25]
	v_ashrrev_i32_e32 v27, 31, v26
	v_ashrrev_i32_e32 v39, 31, v38
	v_ashrrev_i32_e32 v41, 31, v40
	v_ashrrev_i32_e32 v43, 31, v42
	v_lshl_add_u64 v[8:9], v[6:7], 0, v[8:9]
	v_lshlrev_b64 v[10:11], 11, v[10:11]
	v_lshlrev_b64 v[22:23], 11, v[22:23]
	v_lshl_add_u64 v[24:25], v[6:7], 0, v[24:25]
	v_lshlrev_b64 v[26:27], 11, v[26:27]
	v_lshlrev_b64 v[38:39], 11, v[38:39]
	v_lshlrev_b64 v[40:41], 11, v[40:41]
	v_lshlrev_b64 v[42:43], 11, v[42:43]
	v_lshl_add_u64 v[10:11], v[6:7], 0, v[10:11]
	v_lshl_add_u64 v[22:23], v[6:7], 0, v[22:23]
	v_lshl_add_u64 v[26:27], v[6:7], 0, v[26:27]
	v_lshl_add_u64 v[38:39], v[6:7], 0, v[38:39]
	v_lshl_add_u64 v[40:41], v[6:7], 0, v[40:41]
	v_lshl_add_u64 v[42:43], v[6:7], 0, v[42:43]
	global_load_dword v67, v[8:9], off
	global_load_dword v68, v[10:11], off
	global_load_dword v65, v[22:23], off
	global_load_dword v66, v[24:25], off
	global_load_dword v63, v[26:27], off
	global_load_dword v64, v[38:39], off
	global_load_dword v61, v[40:41], off
	global_load_dword v62, v[42:43], off
	v_add_u32_e32 v8, 48, v2
	v_add_u32_e32 v24, 54, v2
	v_ashrrev_i32_e32 v9, 31, v8
	v_add_u32_e32 v10, 50, v2
	v_add_u32_e32 v22, 52, v2
	v_ashrrev_i32_e32 v25, 31, v24
	v_add_u32_e32 v26, 56, v2
	v_add_u32_e32 v38, 58, v2
	v_add_u32_e32 v40, 60, v2
	v_add_u32_e32 v42, 62, v2
	v_lshlrev_b64 v[8:9], 11, v[8:9]
	v_ashrrev_i32_e32 v11, 31, v10
	v_ashrrev_i32_e32 v23, 31, v22
	v_lshlrev_b64 v[24:25], 11, v[24:25]
	v_ashrrev_i32_e32 v27, 31, v26
	v_ashrrev_i32_e32 v39, 31, v38
	v_ashrrev_i32_e32 v41, 31, v40
	v_ashrrev_i32_e32 v43, 31, v42
	v_lshl_add_u64 v[8:9], v[6:7], 0, v[8:9]
	v_lshlrev_b64 v[10:11], 11, v[10:11]
	v_lshlrev_b64 v[22:23], 11, v[22:23]
	v_lshl_add_u64 v[24:25], v[6:7], 0, v[24:25]
	v_lshlrev_b64 v[26:27], 11, v[26:27]
	v_lshlrev_b64 v[38:39], 11, v[38:39]
	v_lshlrev_b64 v[40:41], 11, v[40:41]
	v_lshlrev_b64 v[42:43], 11, v[42:43]
	v_lshl_add_u64 v[10:11], v[6:7], 0, v[10:11]
	v_lshl_add_u64 v[22:23], v[6:7], 0, v[22:23]
	v_lshl_add_u64 v[26:27], v[6:7], 0, v[26:27]
	v_lshl_add_u64 v[38:39], v[6:7], 0, v[38:39]
	v_lshl_add_u64 v[40:41], v[6:7], 0, v[40:41]
	v_lshl_add_u64 v[42:43], v[6:7], 0, v[42:43]
	global_load_dword v102, v[8:9], off
	global_load_dword v103, v[10:11], off
	global_load_dword v100, v[22:23], off
	global_load_dword v101, v[24:25], off
	global_load_dword v98, v[26:27], off
	global_load_dword v99, v[38:39], off
	global_load_dword v94, v[40:41], off
	global_load_dword v95, v[42:43], off
	v_add_u32_e32 v24, 0x46, v2
	v_ashrrev_i32_e32 v25, 31, v24
	v_lshlrev_b64 v[24:25], 11, v[24:25]
	v_lshl_add_u64 v[38:39], v[6:7], 0, v[24:25]
	v_add_u32_e32 v24, 0x48, v2
	v_ashrrev_i32_e32 v25, 31, v24
	v_lshlrev_b64 v[24:25], 11, v[24:25]
	v_lshl_add_u64 v[40:41], v[6:7], 0, v[24:25]
	v_add_u32_e32 v24, 0x4a, v2
	v_ashrrev_i32_e32 v25, 31, v24
	v_lshlrev_b64 v[24:25], 11, v[24:25]
	v_lshl_add_u64 v[42:43], v[6:7], 0, v[24:25]
	v_add_u32_e32 v24, 0x4c, v2
	v_ashrrev_i32_e32 v25, 31, v24
	v_lshlrev_b64 v[24:25], 11, v[24:25]
	v_add_u32_e32 v8, 64, v2
	v_add_u32_e32 v22, 0x44, v2
	v_lshl_add_u64 v[44:45], v[6:7], 0, v[24:25]
	v_add_u32_e32 v24, 0x4e, v2
	v_ashrrev_i32_e32 v9, 31, v8
	v_add_u32_e32 v10, 0x42, v2
	v_ashrrev_i32_e32 v23, 31, v22
	v_ashrrev_i32_e32 v25, 31, v24
	v_lshlrev_b64 v[8:9], 11, v[8:9]
	v_ashrrev_i32_e32 v11, 31, v10
	v_lshlrev_b64 v[22:23], 11, v[22:23]
	v_lshlrev_b64 v[24:25], 11, v[24:25]
	v_lshl_add_u64 v[8:9], v[6:7], 0, v[8:9]
	v_lshlrev_b64 v[10:11], 11, v[10:11]
	v_lshl_add_u64 v[22:23], v[6:7], 0, v[22:23]
	s_waitcnt vmcnt(32)
	v_lshl_add_u64 v[46:47], v[6:7], 0, v[24:25]
	v_lshl_add_u64 v[10:11], v[6:7], 0, v[10:11]
	global_load_dword v27, v[8:9], off
	global_load_dword v28, v[10:11], off
	global_load_dword v25, v[22:23], off
	global_load_dword v26, v[38:39], off
	s_nop 0
	global_load_dword v23, v[40:41], off
	global_load_dword v24, v[42:43], off
	global_load_dword v21, v[44:45], off
	global_load_dword v22, v[46:47], off
	v_add_u32_e32 v46, 0x5c, v2
	v_ashrrev_i32_e32 v47, 31, v46
	v_add_u32_e32 v8, 0x50, v2
	v_add_u32_e32 v40, 0x56, v2
	v_add_u32_e32 v44, 0x5a, v2
	v_lshlrev_b64 v[46:47], 11, v[46:47]
	v_ashrrev_i32_e32 v9, 31, v8
	v_add_u32_e32 v10, 0x52, v2
	v_add_u32_e32 v38, 0x54, v2
	v_ashrrev_i32_e32 v41, 31, v40
	v_add_u32_e32 v42, 0x58, v2
	v_ashrrev_i32_e32 v45, 31, v44
	v_lshl_add_u64 v[54:55], v[6:7], 0, v[46:47]
	v_add_u32_e32 v46, 0x5e, v2
	v_lshlrev_b64 v[8:9], 11, v[8:9]
	v_ashrrev_i32_e32 v11, 31, v10
	v_ashrrev_i32_e32 v39, 31, v38
	v_lshlrev_b64 v[40:41], 11, v[40:41]
	v_ashrrev_i32_e32 v43, 31, v42
	v_lshlrev_b64 v[44:45], 11, v[44:45]
	v_ashrrev_i32_e32 v47, 31, v46
	v_lshl_add_u64 v[8:9], v[6:7], 0, v[8:9]
	v_lshlrev_b64 v[10:11], 11, v[10:11]
	v_lshlrev_b64 v[38:39], 11, v[38:39]
	v_lshl_add_u64 v[40:41], v[6:7], 0, v[40:41]
	v_lshlrev_b64 v[42:43], 11, v[42:43]
	v_lshl_add_u64 v[44:45], v[6:7], 0, v[44:45]
	v_lshlrev_b64 v[46:47], 11, v[46:47]
	v_lshl_add_u64 v[10:11], v[6:7], 0, v[10:11]
	v_lshl_add_u64 v[38:39], v[6:7], 0, v[38:39]
	v_lshl_add_u64 v[42:43], v[6:7], 0, v[42:43]
	v_lshl_add_u64 v[56:57], v[6:7], 0, v[46:47]
	global_load_dword v51, v[8:9], off
	global_load_dword v52, v[10:11], off
	global_load_dword v49, v[38:39], off
	global_load_dword v50, v[40:41], off
	global_load_dword v47, v[42:43], off
	global_load_dword v48, v[44:45], off
	s_nop 0
	global_load_dword v45, v[54:55], off
	global_load_dword v46, v[56:57], off
	v_add_u32_e32 v8, 0x60, v2
	v_add_u32_e32 v40, 0x66, v2
	v_ashrrev_i32_e32 v9, 31, v8
	v_add_u32_e32 v10, 0x62, v2
	v_add_u32_e32 v38, 0x64, v2
	v_ashrrev_i32_e32 v41, 31, v40
	v_add_u32_e32 v42, 0x68, v2
	v_add_u32_e32 v54, 0x6a, v2
	v_add_u32_e32 v56, 0x6c, v2
	v_add_u32_e32 v58, 0x6e, v2
	v_lshlrev_b64 v[8:9], 11, v[8:9]
	v_ashrrev_i32_e32 v11, 31, v10
	v_ashrrev_i32_e32 v39, 31, v38
	v_lshlrev_b64 v[40:41], 11, v[40:41]
	v_ashrrev_i32_e32 v43, 31, v42
	v_ashrrev_i32_e32 v55, 31, v54
	v_ashrrev_i32_e32 v57, 31, v56
	v_ashrrev_i32_e32 v59, 31, v58
	v_lshl_add_u64 v[8:9], v[6:7], 0, v[8:9]
	v_lshlrev_b64 v[10:11], 11, v[10:11]
	v_lshlrev_b64 v[38:39], 11, v[38:39]
	v_lshl_add_u64 v[40:41], v[6:7], 0, v[40:41]
	v_lshlrev_b64 v[42:43], 11, v[42:43]
	v_lshlrev_b64 v[54:55], 11, v[54:55]
	v_lshlrev_b64 v[56:57], 11, v[56:57]
	v_lshlrev_b64 v[58:59], 11, v[58:59]
	v_lshl_add_u64 v[10:11], v[6:7], 0, v[10:11]
	v_lshl_add_u64 v[38:39], v[6:7], 0, v[38:39]
	v_lshl_add_u64 v[42:43], v[6:7], 0, v[42:43]
	v_lshl_add_u64 v[54:55], v[6:7], 0, v[54:55]
	v_lshl_add_u64 v[56:57], v[6:7], 0, v[56:57]
	v_lshl_add_u64 v[58:59], v[6:7], 0, v[58:59]
	global_load_dword v86, v[8:9], off
	global_load_dword v87, v[10:11], off
	global_load_dword v82, v[38:39], off
	global_load_dword v83, v[40:41], off
	global_load_dword v80, v[42:43], off
	global_load_dword v81, v[54:55], off
	global_load_dword v77, v[56:57], off
	global_load_dword v79, v[58:59], off
	v_add_u32_e32 v8, 0x70, v2
	v_add_u32_e32 v40, 0x76, v2
	v_ashrrev_i32_e32 v9, 31, v8
	v_add_u32_e32 v10, 0x72, v2
	v_add_u32_e32 v38, 0x74, v2
	v_ashrrev_i32_e32 v41, 31, v40
	v_add_u32_e32 v42, 0x78, v2
	v_add_u32_e32 v54, 0x7a, v2
	v_add_u32_e32 v56, 0x7c, v2
	v_add_u32_e32 v58, 0x7e, v2
	v_lshlrev_b64 v[8:9], 11, v[8:9]
	v_ashrrev_i32_e32 v11, 31, v10
	v_ashrrev_i32_e32 v39, 31, v38
	v_lshlrev_b64 v[40:41], 11, v[40:41]
	v_ashrrev_i32_e32 v43, 31, v42
	v_ashrrev_i32_e32 v55, 31, v54
	v_ashrrev_i32_e32 v57, 31, v56
	v_ashrrev_i32_e32 v59, 31, v58
	v_lshl_add_u64 v[8:9], v[6:7], 0, v[8:9]
	v_lshlrev_b64 v[10:11], 11, v[10:11]
	v_lshlrev_b64 v[38:39], 11, v[38:39]
	v_lshl_add_u64 v[40:41], v[6:7], 0, v[40:41]
	v_lshlrev_b64 v[42:43], 11, v[42:43]
	v_lshlrev_b64 v[54:55], 11, v[54:55]
	v_lshlrev_b64 v[56:57], 11, v[56:57]
	v_lshlrev_b64 v[58:59], 11, v[58:59]
	v_lshl_add_u64 v[10:11], v[6:7], 0, v[10:11]
	v_lshl_add_u64 v[38:39], v[6:7], 0, v[38:39]
	v_lshl_add_u64 v[42:43], v[6:7], 0, v[42:43]
	v_lshl_add_u64 v[54:55], v[6:7], 0, v[54:55]
	v_lshl_add_u64 v[56:57], v[6:7], 0, v[56:57]
	v_lshl_add_u64 v[58:59], v[6:7], 0, v[58:59]
	global_load_dword v142, v[8:9], off
	global_load_dword v143, v[10:11], off
	global_load_dword v116, v[38:39], off
	global_load_dword v117, v[40:41], off
	global_load_dword v114, v[42:43], off
	global_load_dword v115, v[54:55], off
	global_load_dword v112, v[56:57], off
	global_load_dword v113, v[58:59], off
	v_add_u32_e32 v40, 0x86, v2
	v_ashrrev_i32_e32 v41, 31, v40
	v_lshlrev_b64 v[40:41], 11, v[40:41]
	v_lshl_add_u64 v[54:55], v[6:7], 0, v[40:41]
	v_add_u32_e32 v40, 0x88, v2
	v_ashrrev_i32_e32 v41, 31, v40
	v_lshlrev_b64 v[40:41], 11, v[40:41]
	v_lshl_add_u64 v[56:57], v[6:7], 0, v[40:41]
	v_add_u32_e32 v40, 0x8a, v2
	v_ashrrev_i32_e32 v41, 31, v40
	v_lshlrev_b64 v[40:41], 11, v[40:41]
	v_lshl_add_u64 v[58:59], v[6:7], 0, v[40:41]
	v_add_u32_e32 v40, 0x8c, v2
	v_ashrrev_i32_e32 v41, 31, v40
	v_add_u32_e32 v8, 0x80, v2
	v_add_u32_e32 v38, 0x84, v2
	v_lshlrev_b64 v[40:41], 11, v[40:41]
	v_ashrrev_i32_e32 v9, 31, v8
	v_add_u32_e32 v10, 0x82, v2
	v_ashrrev_i32_e32 v39, 31, v38
	v_lshl_add_u64 v[70:71], v[6:7], 0, v[40:41]
	v_add_u32_e32 v40, 0x8e, v2
	v_lshlrev_b64 v[8:9], 11, v[8:9]
	v_ashrrev_i32_e32 v11, 31, v10
	v_lshlrev_b64 v[38:39], 11, v[38:39]
	v_ashrrev_i32_e32 v41, 31, v40
	v_lshl_add_u64 v[8:9], v[6:7], 0, v[8:9]
	v_lshlrev_b64 v[10:11], 11, v[10:11]
	v_lshl_add_u64 v[38:39], v[6:7], 0, v[38:39]
	v_lshlrev_b64 v[40:41], 11, v[40:41]
	v_lshl_add_u64 v[10:11], v[6:7], 0, v[10:11]
	v_lshl_add_u64 v[72:73], v[6:7], 0, v[40:41]
	global_load_dword v43, v[8:9], off
	global_load_dword v44, v[10:11], off
	global_load_dword v41, v[38:39], off
	global_load_dword v42, v[54:55], off
	s_nop 0
	global_load_dword v39, v[56:57], off
	global_load_dword v40, v[58:59], off
	global_load_dword v37, v[70:71], off
	global_load_dword v38, v[72:73], off
	v_add_u32_e32 v70, 0x9a, v2
	v_ashrrev_i32_e32 v71, 31, v70
	v_lshlrev_b64 v[70:71], 11, v[70:71]
	v_lshl_add_u64 v[84:85], v[6:7], 0, v[70:71]
	v_add_u32_e32 v70, 0x9c, v2
	v_ashrrev_i32_e32 v71, 31, v70
	v_add_u32_e32 v8, 0x90, v2
	v_add_u32_e32 v56, 0x96, v2
	v_lshlrev_b64 v[70:71], 11, v[70:71]
	v_ashrrev_i32_e32 v9, 31, v8
	v_add_u32_e32 v10, 0x92, v2
	v_add_u32_e32 v54, 0x94, v2
	v_ashrrev_i32_e32 v57, 31, v56
	v_add_u32_e32 v58, 0x98, v2
	v_lshl_add_u64 v[88:89], v[6:7], 0, v[70:71]
	v_add_u32_e32 v70, 0x9e, v2
	v_lshlrev_b64 v[8:9], 11, v[8:9]
	v_ashrrev_i32_e32 v11, 31, v10
	v_ashrrev_i32_e32 v55, 31, v54
	v_lshlrev_b64 v[56:57], 11, v[56:57]
	v_ashrrev_i32_e32 v59, 31, v58
	v_ashrrev_i32_e32 v71, 31, v70
	v_lshl_add_u64 v[8:9], v[6:7], 0, v[8:9]
	v_lshlrev_b64 v[10:11], 11, v[10:11]
	v_lshlrev_b64 v[54:55], 11, v[54:55]
	v_lshl_add_u64 v[56:57], v[6:7], 0, v[56:57]
	v_lshlrev_b64 v[58:59], 11, v[58:59]
	v_lshlrev_b64 v[70:71], 11, v[70:71]
	v_lshl_add_u64 v[10:11], v[6:7], 0, v[10:11]
	v_lshl_add_u64 v[54:55], v[6:7], 0, v[54:55]
	v_lshl_add_u64 v[58:59], v[6:7], 0, v[58:59]
	v_lshl_add_u64 v[90:91], v[6:7], 0, v[70:71]
	global_load_dword v75, v[8:9], off
	global_load_dword v76, v[10:11], off
	global_load_dword v73, v[54:55], off
	global_load_dword v74, v[56:57], off
	global_load_dword v71, v[58:59], off
	global_load_dword v72, v[84:85], off
	global_load_dword v69, v[88:89], off
	global_load_dword v70, v[90:91], off
	v_add_u32_e32 v8, 0xa0, v2
	v_add_u32_e32 v56, 0xa6, v2
	v_ashrrev_i32_e32 v9, 31, v8
	v_add_u32_e32 v10, 0xa2, v2
	v_add_u32_e32 v54, 0xa4, v2
	v_ashrrev_i32_e32 v57, 31, v56
	v_add_u32_e32 v58, 0xa8, v2
	v_add_u32_e32 v84, 0xaa, v2
	v_add_u32_e32 v88, 0xac, v2
	v_add_u32_e32 v90, 0xae, v2
	v_lshlrev_b64 v[8:9], 11, v[8:9]
	v_ashrrev_i32_e32 v11, 31, v10
	v_ashrrev_i32_e32 v55, 31, v54
	v_lshlrev_b64 v[56:57], 11, v[56:57]
	v_ashrrev_i32_e32 v59, 31, v58
	v_ashrrev_i32_e32 v85, 31, v84
	v_ashrrev_i32_e32 v89, 31, v88
	v_ashrrev_i32_e32 v91, 31, v90
	v_lshl_add_u64 v[8:9], v[6:7], 0, v[8:9]
	v_lshlrev_b64 v[10:11], 11, v[10:11]
	v_lshlrev_b64 v[54:55], 11, v[54:55]
	v_lshl_add_u64 v[56:57], v[6:7], 0, v[56:57]
	v_lshlrev_b64 v[58:59], 11, v[58:59]
	v_lshlrev_b64 v[84:85], 11, v[84:85]
	v_lshlrev_b64 v[88:89], 11, v[88:89]
	v_lshlrev_b64 v[90:91], 11, v[90:91]
	v_lshl_add_u64 v[10:11], v[6:7], 0, v[10:11]
	v_lshl_add_u64 v[54:55], v[6:7], 0, v[54:55]
	v_lshl_add_u64 v[58:59], v[6:7], 0, v[58:59]
	v_lshl_add_u64 v[84:85], v[6:7], 0, v[84:85]
	v_lshl_add_u64 v[88:89], v[6:7], 0, v[88:89]
	v_lshl_add_u64 v[90:91], v[6:7], 0, v[90:91]
	global_load_dword v110, v[8:9], off
	global_load_dword v111, v[10:11], off
	global_load_dword v108, v[54:55], off
	global_load_dword v109, v[56:57], off
	global_load_dword v106, v[58:59], off
	global_load_dword v107, v[84:85], off
	global_load_dword v104, v[88:89], off
	global_load_dword v105, v[90:91], off
	v_add_u32_e32 v8, 0xb0, v2
	v_add_u32_e32 v56, 0xb6, v2
	v_ashrrev_i32_e32 v9, 31, v8
	v_add_u32_e32 v10, 0xb2, v2
	v_add_u32_e32 v54, 0xb4, v2
	v_ashrrev_i32_e32 v57, 31, v56
	v_add_u32_e32 v58, 0xb8, v2
	v_add_u32_e32 v84, 0xba, v2
	v_add_u32_e32 v88, 0xbc, v2
	v_add_u32_e32 v90, 0xbe, v2
	v_lshlrev_b64 v[8:9], 11, v[8:9]
	v_ashrrev_i32_e32 v11, 31, v10
	v_ashrrev_i32_e32 v55, 31, v54
	v_lshlrev_b64 v[56:57], 11, v[56:57]
	v_ashrrev_i32_e32 v59, 31, v58
	v_ashrrev_i32_e32 v85, 31, v84
	v_ashrrev_i32_e32 v89, 31, v88
	v_ashrrev_i32_e32 v91, 31, v90
	v_lshl_add_u64 v[8:9], v[6:7], 0, v[8:9]
	v_lshlrev_b64 v[10:11], 11, v[10:11]
	v_lshlrev_b64 v[54:55], 11, v[54:55]
	v_lshl_add_u64 v[56:57], v[6:7], 0, v[56:57]
	v_lshlrev_b64 v[58:59], 11, v[58:59]
	v_lshlrev_b64 v[84:85], 11, v[84:85]
	v_lshlrev_b64 v[88:89], 11, v[88:89]
	v_lshlrev_b64 v[90:91], 11, v[90:91]
	v_lshl_add_u64 v[10:11], v[6:7], 0, v[10:11]
	v_lshl_add_u64 v[54:55], v[6:7], 0, v[54:55]
	v_lshl_add_u64 v[58:59], v[6:7], 0, v[58:59]
	v_lshl_add_u64 v[84:85], v[6:7], 0, v[84:85]
	v_lshl_add_u64 v[88:89], v[6:7], 0, v[88:89]
	v_lshl_add_u64 v[90:91], v[6:7], 0, v[90:91]
	global_load_dword v159, v[8:9], off
	global_load_dword v160, v[10:11], off
	global_load_dword v157, v[54:55], off
	global_load_dword v158, v[56:57], off
	global_load_dword v155, v[58:59], off
	global_load_dword v156, v[84:85], off
	global_load_dword v153, v[88:89], off
	global_load_dword v154, v[90:91], off
	v_add_u32_e32 v56, 0xc6, v2
	v_ashrrev_i32_e32 v57, 31, v56
	v_lshlrev_b64 v[56:57], 11, v[56:57]
	v_lshl_add_u64 v[84:85], v[6:7], 0, v[56:57]
	v_add_u32_e32 v56, 0xc8, v2
	v_ashrrev_i32_e32 v57, 31, v56
	v_lshlrev_b64 v[56:57], 11, v[56:57]
	v_lshl_add_u64 v[88:89], v[6:7], 0, v[56:57]
	v_add_u32_e32 v56, 0xca, v2
	v_ashrrev_i32_e32 v57, 31, v56
	v_lshlrev_b64 v[56:57], 11, v[56:57]
	v_lshl_add_u64 v[90:91], v[6:7], 0, v[56:57]
	v_add_u32_e32 v56, 0xcc, v2
	v_ashrrev_i32_e32 v57, 31, v56
	v_add_u32_e32 v8, 0xc0, v2
	v_add_u32_e32 v54, 0xc4, v2
	v_lshlrev_b64 v[56:57], 11, v[56:57]
	v_ashrrev_i32_e32 v9, 31, v8
	v_add_u32_e32 v10, 0xc2, v2
	v_ashrrev_i32_e32 v55, 31, v54
	v_lshl_add_u64 v[92:93], v[6:7], 0, v[56:57]
	v_add_u32_e32 v56, 0xce, v2
	v_lshlrev_b64 v[8:9], 11, v[8:9]
	v_ashrrev_i32_e32 v11, 31, v10
	v_lshlrev_b64 v[54:55], 11, v[54:55]
	v_ashrrev_i32_e32 v57, 31, v56
	v_lshl_add_u64 v[8:9], v[6:7], 0, v[8:9]
	v_lshlrev_b64 v[10:11], 11, v[10:11]
	v_lshl_add_u64 v[54:55], v[6:7], 0, v[54:55]
	v_lshlrev_b64 v[56:57], 11, v[56:57]
	v_lshl_add_u64 v[10:11], v[6:7], 0, v[10:11]
	v_lshl_add_u64 v[96:97], v[6:7], 0, v[56:57]
	global_load_dword v59, v[8:9], off
	global_load_dword v60, v[10:11], off
	global_load_dword v57, v[54:55], off
	global_load_dword v58, v[84:85], off
	s_nop 0
	global_load_dword v55, v[88:89], off
	global_load_dword v56, v[90:91], off
	global_load_dword v53, v[92:93], off
	global_load_dword v54, v[96:97], off
	v_add_u32_e32 v92, 0xda, v2
	v_ashrrev_i32_e32 v93, 31, v92
	v_lshlrev_b64 v[92:93], 11, v[92:93]
	v_lshl_add_u64 v[144:145], v[6:7], 0, v[92:93]
	v_add_u32_e32 v92, 0xdc, v2
	v_ashrrev_i32_e32 v93, 31, v92
	v_lshlrev_b64 v[92:93], 11, v[92:93]
	v_add_u32_e32 v8, 0xd0, v2
	v_add_u32_e32 v88, 0xd6, v2
	v_add_u32_e32 v90, 0xd8, v2
	v_lshl_add_u64 v[146:147], v[6:7], 0, v[92:93]
	v_add_u32_e32 v92, 0xde, v2
	v_ashrrev_i32_e32 v9, 31, v8
	v_add_u32_e32 v10, 0xd2, v2
	v_add_u32_e32 v84, 0xd4, v2
	v_ashrrev_i32_e32 v89, 31, v88
	v_ashrrev_i32_e32 v91, 31, v90
	v_ashrrev_i32_e32 v93, 31, v92
	v_lshlrev_b64 v[8:9], 11, v[8:9]
	v_ashrrev_i32_e32 v11, 31, v10
	v_ashrrev_i32_e32 v85, 31, v84
	v_lshlrev_b64 v[88:89], 11, v[88:89]
	v_lshlrev_b64 v[90:91], 11, v[90:91]
	v_lshlrev_b64 v[92:93], 11, v[92:93]
	v_lshl_add_u64 v[8:9], v[6:7], 0, v[8:9]
	v_lshlrev_b64 v[10:11], 11, v[10:11]
	v_lshlrev_b64 v[84:85], 11, v[84:85]
	v_lshl_add_u64 v[88:89], v[6:7], 0, v[88:89]
	v_lshl_add_u64 v[90:91], v[6:7], 0, v[90:91]
	v_lshl_add_u64 v[148:149], v[6:7], 0, v[92:93]
	v_lshl_add_u64 v[10:11], v[6:7], 0, v[10:11]
	v_lshl_add_u64 v[84:85], v[6:7], 0, v[84:85]
	global_load_dword v96, v[8:9], off
	global_load_dword v97, v[10:11], off
	global_load_dword v92, v[84:85], off
	global_load_dword v93, v[88:89], off
	s_nop 0
	global_load_dword v90, v[90:91], off
	s_nop 0
	global_load_dword v91, v[144:145], off
	global_load_dword v88, v[146:147], off
	global_load_dword v89, v[148:149], off
	v_add_u32_e32 v148, 0xea, v2
	v_ashrrev_i32_e32 v149, 31, v148
	v_lshlrev_b64 v[148:149], 11, v[148:149]
	v_lshl_add_u64 v[162:163], v[6:7], 0, v[148:149]
	v_add_u32_e32 v148, 0xec, v2
	v_ashrrev_i32_e32 v149, 31, v148
	v_add_u32_e32 v8, 0xe0, v2
	v_add_u32_e32 v144, 0xe6, v2
	v_add_u32_e32 v146, 0xe8, v2
	v_lshlrev_b64 v[148:149], 11, v[148:149]
	v_ashrrev_i32_e32 v9, 31, v8
	v_add_u32_e32 v10, 0xe2, v2
	v_add_u32_e32 v84, 0xe4, v2
	v_ashrrev_i32_e32 v145, 31, v144
	v_ashrrev_i32_e32 v147, 31, v146
	v_lshl_add_u64 v[164:165], v[6:7], 0, v[148:149]
	v_add_u32_e32 v148, 0xee, v2
	v_lshlrev_b64 v[8:9], 11, v[8:9]
	v_ashrrev_i32_e32 v11, 31, v10
	v_ashrrev_i32_e32 v85, 31, v84
	v_lshlrev_b64 v[144:145], 11, v[144:145]
	v_lshlrev_b64 v[146:147], 11, v[146:147]
	v_ashrrev_i32_e32 v149, 31, v148
	v_lshl_add_u64 v[8:9], v[6:7], 0, v[8:9]
	v_lshlrev_b64 v[10:11], 11, v[10:11]
	v_lshlrev_b64 v[84:85], 11, v[84:85]
	v_lshl_add_u64 v[144:145], v[6:7], 0, v[144:145]
	v_lshl_add_u64 v[146:147], v[6:7], 0, v[146:147]
	v_lshlrev_b64 v[148:149], 11, v[148:149]
	v_lshl_add_u64 v[10:11], v[6:7], 0, v[10:11]
	v_lshl_add_u64 v[84:85], v[6:7], 0, v[84:85]
	v_lshl_add_u64 v[166:167], v[6:7], 0, v[148:149]
	global_load_dword v150, v[8:9], off
	global_load_dword v151, v[10:11], off
	global_load_dword v148, v[84:85], off
	global_load_dword v149, v[144:145], off
	s_nop 0
	global_load_dword v146, v[146:147], off
	s_nop 0
	global_load_dword v147, v[162:163], off
	global_load_dword v144, v[164:165], off
	global_load_dword v145, v[166:167], off
	v_add_u32_e32 v164, 0xf8, v2
	v_ashrrev_i32_e32 v165, 31, v164
	v_lshlrev_b64 v[164:165], 11, v[164:165]
	v_lshl_add_u64 v[170:171], v[6:7], 0, v[164:165]
	v_add_u32_e32 v164, 0xfa, v2
	v_ashrrev_i32_e32 v165, 31, v164
	v_add_u32_e32 v8, 0xf0, v2
	v_add_u32_e32 v162, 0xf6, v2
	v_lshlrev_b64 v[164:165], 11, v[164:165]
	v_ashrrev_i32_e32 v9, 31, v8
	v_add_u32_e32 v10, 0xf2, v2
	v_add_u32_e32 v84, 0xf4, v2
	v_ashrrev_i32_e32 v163, 31, v162
	v_lshl_add_u64 v[172:173], v[6:7], 0, v[164:165]
	v_add_u32_e32 v164, 0xfc, v2
	v_add_u32_e32 v2, 0xfe, v2
	v_lshlrev_b64 v[8:9], 11, v[8:9]
	v_ashrrev_i32_e32 v11, 31, v10
	v_ashrrev_i32_e32 v85, 31, v84
	v_lshlrev_b64 v[162:163], 11, v[162:163]
	v_ashrrev_i32_e32 v165, 31, v164
	v_ashrrev_i32_e32 v3, 31, v2
	v_lshl_add_u64 v[8:9], v[6:7], 0, v[8:9]
	v_lshlrev_b64 v[10:11], 11, v[10:11]
	v_lshlrev_b64 v[84:85], 11, v[84:85]
	v_lshl_add_u64 v[162:163], v[6:7], 0, v[162:163]
	v_lshlrev_b64 v[164:165], 11, v[164:165]
	v_lshlrev_b64 v[2:3], 11, v[2:3]
	v_lshl_add_u64 v[10:11], v[6:7], 0, v[10:11]
	v_lshl_add_u64 v[84:85], v[6:7], 0, v[84:85]
	v_lshl_add_u64 v[174:175], v[6:7], 0, v[164:165]
	v_lshl_add_u64 v[2:3], v[6:7], 0, v[2:3]
	global_load_dword v167, v[8:9], off
	global_load_dword v168, v[10:11], off
	global_load_dword v165, v[84:85], off
	global_load_dword v166, v[162:163], off
	s_nop 0
	global_load_dword v163, v[170:171], off
	global_load_dword v164, v[172:173], off
	global_load_dword v161, v[174:175], off
	global_load_dword v162, v[2:3], off
	s_waitcnt vmcnt(62)
	v_max3_f32 v2, |v18|, 0, |v19|
	v_max3_f32 v2, v2, |v16|, |v17|
	v_max3_f32 v2, v2, |v14|, |v15|
	v_max3_f32 v2, v2, |v12|, |v13|
	v_max3_f32 v2, v2, |v35|, |v36|
	v_max3_f32 v2, v2, |v33|, |v34|
	v_max3_f32 v2, v2, |v31|, |v32|
	v_max3_f32 v2, v2, |v29|, |v30|
	v_max3_f32 v2, v2, |v67|, |v68|
	v_max3_f32 v2, v2, |v65|, |v66|
	v_max3_f32 v2, v2, |v63|, |v64|
	v_max3_f32 v2, v2, |v61|, |v62|
	v_max3_f32 v2, v2, |v102|, |v103|
	v_max3_f32 v2, v2, |v100|, |v101|
	v_max3_f32 v2, v2, |v98|, |v99|
	v_max3_f32 v2, v2, |v94|, |v95|
	v_max3_f32 v2, v2, |v27|, |v28|
	v_max3_f32 v2, v2, |v25|, |v26|
	v_max3_f32 v2, v2, |v23|, |v24|
	v_max3_f32 v2, v2, |v21|, |v22|
	v_max3_f32 v2, v2, |v51|, |v52|
	v_max3_f32 v2, v2, |v49|, |v50|
	v_max3_f32 v2, v2, |v47|, |v48|
	v_max3_f32 v2, v2, |v45|, |v46|
	v_max3_f32 v2, v2, |v86|, |v87|
	v_max3_f32 v2, v2, |v82|, |v83|
	v_max3_f32 v2, v2, |v80|, |v81|
	v_max3_f32 v2, v2, |v77|, |v79|
	v_max3_f32 v2, v2, |v142|, |v143|
	v_max3_f32 v2, v2, |v116|, |v117|
	v_max3_f32 v2, v2, |v114|, |v115|
	v_max3_f32 v2, v2, |v112|, |v113|
	v_max3_f32 v2, v2, |v43|, |v44|
	s_waitcnt vmcnt(60)
	v_max3_f32 v2, v2, |v41|, |v42|
	s_waitcnt vmcnt(58)
	v_max3_f32 v2, v2, |v39|, |v40|
	s_waitcnt vmcnt(56)
	v_max3_f32 v2, v2, |v37|, |v38|
	s_waitcnt vmcnt(54)
	v_max3_f32 v2, v2, |v75|, |v76|
	s_waitcnt vmcnt(52)
	v_max3_f32 v2, v2, |v73|, |v74|
	s_waitcnt vmcnt(50)
	v_max3_f32 v2, v2, |v71|, |v72|
	s_waitcnt vmcnt(48)
	v_max3_f32 v2, v2, |v69|, |v70|
	s_waitcnt vmcnt(46)
	v_max3_f32 v2, v2, |v110|, |v111|
	s_waitcnt vmcnt(44)
	v_max3_f32 v2, v2, |v108|, |v109|
	s_waitcnt vmcnt(42)
	v_max3_f32 v2, v2, |v106|, |v107|
	s_waitcnt vmcnt(40)
	v_max3_f32 v2, v2, |v104|, |v105|
	s_waitcnt vmcnt(38)
	v_max3_f32 v2, v2, |v159|, |v160|
	s_waitcnt vmcnt(36)
	v_max3_f32 v2, v2, |v157|, |v158|
	s_waitcnt vmcnt(34)
	v_max3_f32 v2, v2, |v155|, |v156|
	s_waitcnt vmcnt(32)
	v_max3_f32 v2, v2, |v153|, |v154|
	s_waitcnt vmcnt(30)
	v_max3_f32 v2, v2, |v59|, |v60|
	s_waitcnt vmcnt(28)
	v_max3_f32 v2, v2, |v57|, |v58|
	s_waitcnt vmcnt(26)
	v_max3_f32 v2, v2, |v55|, |v56|
	s_waitcnt vmcnt(24)
	v_max3_f32 v2, v2, |v53|, |v54|
	s_waitcnt vmcnt(22)
	v_max3_f32 v2, v2, |v96|, |v97|
	s_waitcnt vmcnt(20)
	v_max3_f32 v2, v2, |v92|, |v93|
	s_waitcnt vmcnt(18)
	v_max3_f32 v2, v2, |v90|, |v91|
	s_waitcnt vmcnt(16)
	v_max3_f32 v2, v2, |v88|, |v89|
	s_waitcnt vmcnt(14)
	v_max3_f32 v2, v2, |v150|, |v151|
	s_waitcnt vmcnt(12)
	v_max3_f32 v2, v2, |v148|, |v149|
	s_waitcnt vmcnt(10)
	v_max3_f32 v2, v2, |v146|, |v147|
	s_waitcnt vmcnt(8)
	v_max3_f32 v2, v2, |v144|, |v145|
	v_cmp_gt_i32_e32 vcc, 32, v4
	s_barrier
	s_waitcnt vmcnt(6)
	v_max3_f32 v2, v2, |v167|, |v168|
	s_waitcnt vmcnt(4)
	v_max3_f32 v2, v2, |v165|, |v166|
	s_waitcnt vmcnt(2)
	v_max3_f32 v2, v2, |v163|, |v164|
	s_waitcnt vmcnt(0)
	v_max3_f32 v2, v2, |v161|, |v162|
	ds_bpermute_b32 v3, v121, v2
	s_and_saveexec_b64 s[14:15], vcc
	s_cbranch_execz .LBB0_1222
	s_waitcnt lgkmcnt(0)
	v_max_f32_e32 v3, v3, v3
	v_max_f32_e32 v2, v2, v2
	v_lshl_add_u32 v6, v4, 2, s33
	v_max_f32_e32 v2, v2, v3
	ds_write_b32 v6, v2
